# pass-B cache-warming wave keeps four steps of P/Q requests in flight (runs ahead of the chain)
# speedup vs baseline: 1.0037x; 1.0037x over previous
.Lcbh_step:
	global_load_dwordx4 v[2:5], v9, s[32:33]
	global_load_dwordx4 v[2:5], v9, s[32:33] offset:1024
	global_load_dwordx4 v[2:5], v9, s[32:33] offset:2048
	global_load_dwordx4 v[2:5], v9, s[32:33] offset:3072
	global_load_dwordx4 v[2:5], v10, s[32:33]
	global_load_dwordx4 v[2:5], v10, s[32:33] offset:1024
	global_load_dwordx4 v[2:5], v10, s[32:33] offset:2048
	global_load_dwordx4 v[2:5], v10, s[32:33] offset:3072
	global_load_dwordx4 v[2:5], v11, s[34:35]
	global_load_dwordx4 v[2:5], v12, s[34:35]
	global_load_dwordx4 v[2:5], v13, s[34:35]
	global_load_dwordx4 v[2:5], v50, s[34:35]
	s_add_u32 s32, s32, 0x2000
	s_addc_u32 s33, s33, 0
	s_add_u32 s34, s34, 0x4000
	s_addc_u32 s35, s35, 0
	s_waitcnt vmcnt(48)
	s_sub_i32 s29, s29, 1
	s_cmp_lg_u32 s29, 0
	s_cbranch_scc1 .Lcbh_step
	s_add_i32 s28, s28, s0
	s_branch .Lcbh_unit
